# speedup vs baseline: 1.0432x; 1.0072x over previous
.LBB1_11:
	s_waitcnt lgkmcnt(0)
	s_waitcnt lgkmcnt(0)
	s_barrier
	v_add_u32_e32 v110, s3, v1
	v_add_u32_e32 v134, s3, v152
	ds_read_b128 v[98:101], v110
	ds_read_b128 v[102:105], v110 offset:1024
	ds_read_b128 v[106:109], v110 offset:2048
	ds_read_b128 v[110:113], v110 offset:3072
	ds_read_b128 v[114:117], v134 offset:16384
	ds_read_b128 v[118:121], v134 offset:17408
	ds_read_b128 v[122:125], v134 offset:18432
	ds_read_b128 v[126:129], v134 offset:19456
	ds_read_b128 v[130:133], v134 offset:20480
	ds_read_b128 v[134:137], v134 offset:21504
	s_addk_i32 s3, 0x7000
	s_barrier
	s_setprio 1
	s_waitcnt lgkmcnt(5)
	v_mfma_f32_16x16x32_f16 v[94:97], v[114:117], v[98:101], v[94:97]
	s_cmp_lg_u32 s3, 0x23000
	s_cselect_b32 s3, s3, 0
	s_waitcnt lgkmcnt(4)
	v_mfma_f32_16x16x32_f16 v[90:93], v[118:121], v[98:101], v[90:93]
	s_waitcnt lgkmcnt(3)
	v_mfma_f32_16x16x32_f16 v[86:89], v[122:125], v[98:101], v[86:89]
	s_waitcnt lgkmcnt(2)
	v_mfma_f32_16x16x32_f16 v[82:85], v[126:129], v[98:101], v[82:85]
	s_waitcnt lgkmcnt(1)
	v_mfma_f32_16x16x32_f16 v[78:81], v[130:133], v[98:101], v[78:81]
	s_waitcnt lgkmcnt(0)
	v_mfma_f32_16x16x32_f16 v[74:77], v[134:137], v[98:101], v[74:77]
	v_mfma_f32_16x16x32_f16 v[70:73], v[114:117], v[102:105], v[70:73]
	v_mfma_f32_16x16x32_f16 v[66:69], v[118:121], v[102:105], v[66:69]
	v_mfma_f32_16x16x32_f16 v[62:65], v[122:125], v[102:105], v[62:65]
	v_mfma_f32_16x16x32_f16 v[58:61], v[126:129], v[102:105], v[58:61]
	v_mfma_f32_16x16x32_f16 v[54:57], v[130:133], v[102:105], v[54:57]
	v_mfma_f32_16x16x32_f16 v[50:53], v[134:137], v[102:105], v[50:53]
	v_mfma_f32_16x16x32_f16 v[46:49], v[114:117], v[106:109], v[46:49]
	v_mfma_f32_16x16x32_f16 v[42:45], v[118:121], v[106:109], v[42:45]
	v_mfma_f32_16x16x32_f16 v[38:41], v[122:125], v[106:109], v[38:41]
	v_mfma_f32_16x16x32_f16 v[34:37], v[126:129], v[106:109], v[34:37]
	v_mfma_f32_16x16x32_f16 v[30:33], v[130:133], v[106:109], v[30:33]
	v_mfma_f32_16x16x32_f16 v[26:29], v[134:137], v[106:109], v[26:29]
	v_mfma_f32_16x16x32_f16 v[22:25], v[114:117], v[110:113], v[22:25]
	v_mfma_f32_16x16x32_f16 v[18:21], v[118:121], v[110:113], v[18:21]
	v_mfma_f32_16x16x32_f16 v[14:17], v[122:125], v[110:113], v[14:17]
	v_mfma_f32_16x16x32_f16 v[10:13], v[126:129], v[110:113], v[10:13]
	v_mfma_f32_16x16x32_f16 v[6:9], v[130:133], v[110:113], v[6:9]
	v_mfma_f32_16x16x32_f16 v[2:5], v[134:137], v[110:113], v[2:5]
	s_setprio 0
	s_waitcnt lgkmcnt(0)
	s_waitcnt lgkmcnt(0)
	s_barrier
	v_add_u32_e32 v110, s3, v1
	v_add_u32_e32 v134, s3, v152
	ds_read_b128 v[98:101], v110
	ds_read_b128 v[102:105], v110 offset:1024
	ds_read_b128 v[106:109], v110 offset:2048
	ds_read_b128 v[110:113], v110 offset:3072
	ds_read_b128 v[114:117], v134 offset:16384
	ds_read_b128 v[118:121], v134 offset:17408
	ds_read_b128 v[122:125], v134 offset:18432
	ds_read_b128 v[126:129], v134 offset:19456
	ds_read_b128 v[130:133], v134 offset:20480
	ds_read_b128 v[134:137], v134 offset:21504
	s_addk_i32 s3, 0x7000
	s_barrier
	s_setprio 1
	s_waitcnt lgkmcnt(5)
	v_mfma_f32_16x16x32_f16 v[94:97], v[114:117], v[98:101], v[94:97]
	s_cmp_lg_u32 s3, 0x23000
	s_cselect_b32 s3, s3, 0
	s_waitcnt lgkmcnt(4)
	v_mfma_f32_16x16x32_f16 v[90:93], v[118:121], v[98:101], v[90:93]
	s_waitcnt lgkmcnt(3)
	v_mfma_f32_16x16x32_f16 v[86:89], v[122:125], v[98:101], v[86:89]
	s_waitcnt lgkmcnt(2)
	v_mfma_f32_16x16x32_f16 v[82:85], v[126:129], v[98:101], v[82:85]
	s_waitcnt lgkmcnt(1)
	v_mfma_f32_16x16x32_f16 v[78:81], v[130:133], v[98:101], v[78:81]
	s_waitcnt lgkmcnt(0)
	v_mfma_f32_16x16x32_f16 v[74:77], v[134:137], v[98:101], v[74:77]
	v_mfma_f32_16x16x32_f16 v[70:73], v[114:117], v[102:105], v[70:73]
	v_mfma_f32_16x16x32_f16 v[66:69], v[118:121], v[102:105], v[66:69]
	v_mfma_f32_16x16x32_f16 v[62:65], v[122:125], v[102:105], v[62:65]
	v_mfma_f32_16x16x32_f16 v[58:61], v[126:129], v[102:105], v[58:61]
	v_mfma_f32_16x16x32_f16 v[54:57], v[130:133], v[102:105], v[54:57]
	v_mfma_f32_16x16x32_f16 v[50:53], v[134:137], v[102:105], v[50:53]
	v_mfma_f32_16x16x32_f16 v[46:49], v[114:117], v[106:109], v[46:49]
	v_mfma_f32_16x16x32_f16 v[42:45], v[118:121], v[106:109], v[42:45]
	v_mfma_f32_16x16x32_f16 v[38:41], v[122:125], v[106:109], v[38:41]
	v_mfma_f32_16x16x32_f16 v[34:37], v[126:129], v[106:109], v[34:37]
	v_mfma_f32_16x16x32_f16 v[30:33], v[130:133], v[106:109], v[30:33]
	v_mfma_f32_16x16x32_f16 v[26:29], v[134:137], v[106:109], v[26:29]
	v_mfma_f32_16x16x32_f16 v[22:25], v[114:117], v[110:113], v[22:25]
	v_mfma_f32_16x16x32_f16 v[18:21], v[118:121], v[110:113], v[18:21]
	v_mfma_f32_16x16x32_f16 v[14:17], v[122:125], v[110:113], v[14:17]
	v_mfma_f32_16x16x32_f16 v[10:13], v[126:129], v[110:113], v[10:13]
	v_mfma_f32_16x16x32_f16 v[6:9], v[130:133], v[110:113], v[6:9]
	v_mfma_f32_16x16x32_f16 v[2:5], v[134:137], v[110:113], v[2:5]
	s_setprio 0
	s_add_i32 s2, s2, -2
	s_cmp_eq_u32 s2, 0
	s_cbranch_scc0 .LBB1_11
	s_waitcnt lgkmcnt(0)
	s_barrier
	s_lshl_b32 s2, s17, 6
	s_or_b32 s2, s2, s18
	s_add_i32 s14, s16, s10
	s_cmpk_lt_i32 s14, 0x400
	s_cselect_b64 vcc, -1, 0
	s_ashr_i32 s12, s14, 10
	v_or_b32_e32 v99, s2, v153
	s_lshr_b32 s2, s2, 7
	s_ashr_i32 s13, s12, 31
	s_and_b32 s15, s2, 0xf0
	s_bfe_u32 s18, s14, 0x40006
	s_lshl_b64 s[12:13], s[12:13], 24
	s_add_u32 s19, s4, s12
	v_mov_b32_e32 v102, s7
	v_mov_b32_e32 v103, s6
	s_addc_u32 s20, s5, s13
	s_or_b32 s12, s15, s18
	v_cndmask_b32_e32 v98, v102, v103, vcc
	v_lshlrev_b32_e32 v99, 6, v99
	s_lshl_b32 s12, s12, 18
	v_lshlrev_b32_e32 v155, 3, v154
	v_mov_b32_e32 v139, 0
	v_and_b32_e32 v142, 0x1f3c0, v99
	v_pk_mul_f32 v[96:97], v[98:99], v[96:97] op_sel_hi:[0,1]
	s_add_u32 s12, s19, s12
	v_pk_mul_f32 v[94:95], v[98:99], v[94:95] op_sel_hi:[0,1]
	v_pk_mul_f32 v[100:101], v[98:99], v[92:93] op_sel_hi:[0,1]
	v_pk_mul_f32 v[90:91], v[98:99], v[90:91] op_sel_hi:[0,1]
	v_cvt_pk_f16_f32 v93, v96, v97
	v_and_or_b32 v144, s16, 32, v155
	s_addc_u32 s13, s20, 0
	v_lshlrev_b32_e32 v96, 1, v142
	v_mov_b32_e32 v97, v139
	s_add_i32 s21, s14, 32
	v_cvt_pk_f16_f32 v92, v94, v95
	v_cvt_pk_f16_f32 v94, v90, v91
	v_cvt_pk_f16_f32 v95, v100, v101
	v_lshl_add_u64 v[100:101], s[12:13], 0, v[96:97]
	v_lshlrev_b32_e32 v90, 1, v144
	v_mov_b32_e32 v91, v139
	s_cmpk_lt_i32 s14, 0x3e0
	v_lshl_add_u64 v[100:101], v[100:101], 0, v[90:91]
	s_cselect_b64 vcc, -1, 0
	s_ashr_i32 s12, s21, 10
	global_store_dwordx4 v[100:101], v[92:95], off sc1
	s_ashr_i32 s13, s12, 31
	s_bfe_u32 s22, s21, 0x40006
	v_cndmask_b32_e32 v92, v102, v103, vcc
	v_pk_mul_f32 v[88:89], v[92:93], v[88:89] op_sel_hi:[0,1]
	v_pk_mul_f32 v[86:87], v[92:93], v[86:87] op_sel_hi:[0,1]
	v_pk_mul_f32 v[84:85], v[92:93], v[84:85] op_sel_hi:[0,1]
	s_lshl_b64 s[12:13], s[12:13], 24
	v_cvt_pk_f16_f32 v86, v86, v87
	v_cvt_pk_f16_f32 v87, v88, v89
	v_cvt_pk_f16_f32 v89, v84, v85
	v_and_or_b32 v84, s21, 32, v155
	s_add_u32 s21, s4, s12
	s_addc_u32 s23, s5, s13
	s_or_b32 s12, s15, s22
	s_lshl_b32 s12, s12, 18
	s_add_u32 s12, s21, s12
	s_addc_u32 s13, s23, 0
	s_add_i32 s24, s14, 64
	v_pk_mul_f32 v[82:83], v[92:93], v[82:83] op_sel_hi:[0,1]
	s_cmpk_lt_i32 s14, 0x3c0
	v_cvt_pk_f16_f32 v88, v82, v83
	v_lshl_add_u64 v[82:83], s[12:13], 0, v[96:97]
	s_cselect_b64 vcc, -1, 0
	s_ashr_i32 s12, s24, 10
	s_ashr_i32 s13, s12, 31
	s_bfe_u32 s24, s24, 0x40006
	s_lshl_b64 s[12:13], s[12:13], 24
	s_add_u32 s25, s4, s12
	v_lshlrev_b32_e32 v84, 1, v84
	v_mov_b32_e32 v85, v139
	s_addc_u32 s26, s5, s13
	s_or_b32 s12, s15, s24
	v_lshl_add_u64 v[82:83], v[82:83], 0, v[84:85]
	s_lshl_b32 s12, s12, 18
	global_store_dwordx4 v[82:83], v[86:89], off sc1
	v_cndmask_b32_e32 v82, v102, v103, vcc
	s_add_u32 s12, s25, s12
	s_mov_b32 s3, 0
	v_pk_mul_f32 v[78:79], v[82:83], v[78:79] op_sel_hi:[0,1]
	s_addc_u32 s13, s26, 0
	s_and_b32 s2, s2, 0xfffff0
	v_pk_mul_f32 v[86:87], v[82:83], v[76:77] op_sel_hi:[0,1]
	v_pk_mul_f32 v[76:77], v[82:83], v[74:75] op_sel_hi:[0,1]
	v_cvt_pk_f16_f32 v74, v78, v79
	v_lshl_add_u64 v[78:79], s[12:13], 0, v[96:97]
	s_or_b32 s12, s2, s18
	s_mov_b32 s13, s3
	v_pk_mul_f32 v[80:81], v[82:83], v[80:81] op_sel_hi:[0,1]
	s_lshl_b64 s[12:13], s[12:13], 18
	v_cvt_pk_f16_f32 v75, v80, v81
	v_cvt_pk_f16_f32 v76, v76, v77
	v_cvt_pk_f16_f32 v77, v86, v87
	v_lshl_add_u64 v[78:79], v[78:79], 0, v[90:91]
	s_add_u32 s12, s19, s12
	v_mov_b32_e32 v138, s15
	global_store_dwordx4 v[78:79], v[74:77], off sc1
	s_mov_b32 s27, 0x1ffc0
	s_addc_u32 s13, s20, s13
	v_mov_b32_e32 v74, 0x400
	s_or_b32 s14, s2, s22
	s_mov_b32 s15, s3
	v_bitop3_b32 v146, v99, s27, v74 bitop3:0xc8
	v_pk_mul_f32 v[70:71], v[98:99], v[70:71] op_sel_hi:[0,1]
	s_lshl_b64 s[14:15], s[14:15], 18
	v_pk_mul_f32 v[72:73], v[98:99], v[72:73] op_sel_hi:[0,1]
	v_pk_mul_f32 v[74:75], v[98:99], v[68:69] op_sel_hi:[0,1]
	v_pk_mul_f32 v[68:69], v[98:99], v[66:67] op_sel_hi:[0,1]
	v_cvt_pk_f16_f32 v66, v70, v71
	v_lshlrev_b32_e32 v70, 1, v146
	v_mov_b32_e32 v71, v139
	s_add_u32 s14, s21, s14
	v_mov_b64_e32 v[140:141], s[2:3]
	v_cvt_pk_f16_f32 v67, v72, v73
	v_lshl_add_u64 v[72:73], s[12:13], 0, v[70:71]
	s_addc_u32 s15, s23, s15
	s_or_b32 s2, s2, s24
	v_cvt_pk_f16_f32 v68, v68, v69
	v_cvt_pk_f16_f32 v69, v74, v75
	v_lshl_add_u64 v[72:73], v[72:73], 0, v[90:91]
	v_pk_mul_f32 v[62:63], v[92:93], v[62:63] op_sel_hi:[0,1]
	s_lshl_b64 s[2:3], s[2:3], 18
	global_store_dwordx4 v[72:73], v[66:69], off sc1
	v_pk_mul_f32 v[64:65], v[92:93], v[64:65] op_sel_hi:[0,1]
	s_add_u32 s2, s25, s2
	v_pk_mul_f32 v[66:67], v[92:93], v[60:61] op_sel_hi:[0,1]
	v_pk_mul_f32 v[60:61], v[92:93], v[58:59] op_sel_hi:[0,1]
	v_cvt_pk_f16_f32 v58, v62, v63
	v_lshl_add_u64 v[62:63], s[14:15], 0, v[70:71]
	v_cvt_pk_f16_f32 v59, v64, v65
	v_cvt_pk_f16_f32 v60, v60, v61
	v_cvt_pk_f16_f32 v61, v66, v67
	v_lshl_add_u64 v[62:63], v[62:63], 0, v[84:85]
	v_pk_mul_f32 v[54:55], v[82:83], v[54:55] op_sel_hi:[0,1]
	s_addc_u32 s3, s26, s3
	global_store_dwordx4 v[62:63], v[58:61], off sc1
	v_pk_mul_f32 v[56:57], v[82:83], v[56:57] op_sel_hi:[0,1]
	v_pk_mul_f32 v[46:47], v[98:99], v[46:47] op_sel_hi:[0,1]
	v_pk_mul_f32 v[58:59], v[82:83], v[52:53] op_sel_hi:[0,1]
	v_pk_mul_f32 v[52:53], v[82:83], v[50:51] op_sel_hi:[0,1]
	v_cvt_pk_f16_f32 v50, v54, v55
	v_lshl_add_u64 v[54:55], s[2:3], 0, v[70:71]
	v_cvt_pk_f16_f32 v51, v56, v57
	v_cvt_pk_f16_f32 v52, v52, v53
	v_cvt_pk_f16_f32 v53, v58, v59
	v_lshl_add_u64 v[54:55], v[54:55], 0, v[90:91]
	global_store_dwordx4 v[54:55], v[50:53], off sc1
	v_pk_mul_f32 v[48:49], v[98:99], v[48:49] op_sel_hi:[0,1]
	v_pk_mul_f32 v[38:39], v[92:93], v[38:39] op_sel_hi:[0,1]
	v_mov_b32_e32 v50, 0x800
	v_bitop3_b32 v148, v99, s27, v50 bitop3:0xc8
	v_pk_mul_f32 v[50:51], v[98:99], v[44:45] op_sel_hi:[0,1]
	v_pk_mul_f32 v[44:45], v[98:99], v[42:43] op_sel_hi:[0,1]
	v_cvt_pk_f16_f32 v42, v46, v47
	v_lshlrev_b32_e32 v46, 1, v148
	v_mov_b32_e32 v47, v139
	v_cvt_pk_f16_f32 v43, v48, v49
	v_lshl_add_u64 v[48:49], s[12:13], 0, v[46:47]
	v_cvt_pk_f16_f32 v44, v44, v45
	v_cvt_pk_f16_f32 v45, v50, v51
	v_lshl_add_u64 v[48:49], v[48:49], 0, v[90:91]
	global_store_dwordx4 v[48:49], v[42:45], off sc1
	v_pk_mul_f32 v[40:41], v[92:93], v[40:41] op_sel_hi:[0,1]
	v_pk_mul_f32 v[30:31], v[82:83], v[30:31] op_sel_hi:[0,1]
	v_pk_mul_f32 v[42:43], v[92:93], v[36:37] op_sel_hi:[0,1]
	v_pk_mul_f32 v[36:37], v[92:93], v[34:35] op_sel_hi:[0,1]
	v_cvt_pk_f16_f32 v34, v38, v39
	v_lshl_add_u64 v[38:39], s[14:15], 0, v[46:47]
	v_cvt_pk_f16_f32 v35, v40, v41
	v_cvt_pk_f16_f32 v36, v36, v37
	v_cvt_pk_f16_f32 v37, v42, v43
	v_lshl_add_u64 v[38:39], v[38:39], 0, v[84:85]
	global_store_dwordx4 v[38:39], v[34:37], off sc1
	v_pk_mul_f32 v[32:33], v[82:83], v[32:33] op_sel_hi:[0,1]
	v_pk_mul_f32 v[22:23], v[98:99], v[22:23] op_sel_hi:[0,1]
	v_pk_mul_f32 v[34:35], v[82:83], v[28:29] op_sel_hi:[0,1]
	v_pk_mul_f32 v[28:29], v[82:83], v[26:27] op_sel_hi:[0,1]
	v_cvt_pk_f16_f32 v26, v30, v31
	v_lshl_add_u64 v[30:31], s[2:3], 0, v[46:47]
	v_cvt_pk_f16_f32 v27, v32, v33
	v_cvt_pk_f16_f32 v28, v28, v29
	v_cvt_pk_f16_f32 v29, v34, v35
	v_lshl_add_u64 v[30:31], v[30:31], 0, v[90:91]
	global_store_dwordx4 v[30:31], v[26:29], off sc1
	v_pk_mul_f32 v[24:25], v[98:99], v[24:25] op_sel_hi:[0,1]
	v_pk_mul_f32 v[14:15], v[92:93], v[14:15] op_sel_hi:[0,1]
	v_mov_b32_e32 v26, 0xc00
	v_bitop3_b32 v150, v99, s27, v26 bitop3:0xc8
	v_pk_mul_f32 v[26:27], v[98:99], v[20:21] op_sel_hi:[0,1]
	v_pk_mul_f32 v[20:21], v[98:99], v[18:19] op_sel_hi:[0,1]
	v_cvt_pk_f16_f32 v18, v22, v23
	v_lshlrev_b32_e32 v22, 1, v150
	v_mov_b32_e32 v23, v139
	v_cvt_pk_f16_f32 v19, v24, v25
	v_lshl_add_u64 v[24:25], s[12:13], 0, v[22:23]
	v_cvt_pk_f16_f32 v20, v20, v21
	v_cvt_pk_f16_f32 v21, v26, v27
	v_lshl_add_u64 v[24:25], v[24:25], 0, v[90:91]
	global_store_dwordx4 v[24:25], v[18:21], off sc1
	v_pk_mul_f32 v[16:17], v[92:93], v[16:17] op_sel_hi:[0,1]
	v_pk_mul_f32 v[6:7], v[82:83], v[6:7] op_sel_hi:[0,1]
	v_pk_mul_f32 v[18:19], v[92:93], v[12:13] op_sel_hi:[0,1]
	v_pk_mul_f32 v[12:13], v[92:93], v[10:11] op_sel_hi:[0,1]
	v_cvt_pk_f16_f32 v10, v14, v15
	v_lshl_add_u64 v[14:15], s[14:15], 0, v[22:23]
	v_cvt_pk_f16_f32 v11, v16, v17
	v_cvt_pk_f16_f32 v12, v12, v13
	v_cvt_pk_f16_f32 v13, v18, v19
	v_lshl_add_u64 v[14:15], v[14:15], 0, v[84:85]
	global_store_dwordx4 v[14:15], v[10:13], off sc1
	v_pk_mul_f32 v[8:9], v[82:83], v[8:9] op_sel_hi:[0,1]
	v_mov_b32_e32 v143, v139
	v_pk_mul_f32 v[10:11], v[82:83], v[4:5] op_sel_hi:[0,1]
	v_pk_mul_f32 v[4:5], v[82:83], v[2:3] op_sel_hi:[0,1]
	v_cvt_pk_f16_f32 v2, v6, v7
	v_lshl_add_u64 v[6:7], s[2:3], 0, v[22:23]
	v_cvt_pk_f16_f32 v3, v8, v9
	v_cvt_pk_f16_f32 v4, v4, v5
	v_cvt_pk_f16_f32 v5, v10, v11
	v_lshl_add_u64 v[6:7], v[6:7], 0, v[90:91]
	s_mov_b32 s17, 32
	v_mov_b32_e32 v145, v139
	v_mov_b32_e32 v147, v139
	v_mov_b32_e32 v149, v139
	v_mov_b32_e32 v151, v139
	global_store_dwordx4 v[6:7], v[2:5], off sc1
	s_mov_b32 s2, 0xe000
	v_mov_b32_e32 v6, v139
	v_mov_b32_e32 v2, v139
	v_mov_b32_e32 v3, v139
	v_mov_b32_e32 v4, v139
	v_mov_b32_e32 v5, v139
	v_mov_b32_e32 v7, v139
	v_mov_b32_e32 v8, v139
	v_mov_b32_e32 v9, v139
	v_mov_b32_e32 v10, v139
	v_mov_b32_e32 v11, v139
	v_mov_b32_e32 v12, v139
	v_mov_b32_e32 v13, v139
	v_mov_b32_e32 v14, v139
	v_mov_b32_e32 v15, v139
	v_mov_b32_e32 v16, v139
	v_mov_b32_e32 v17, v139
	v_mov_b32_e32 v18, v139
	v_mov_b32_e32 v19, v139
	v_mov_b32_e32 v20, v139
	v_mov_b32_e32 v21, v139
	v_mov_b32_e32 v22, v139
	v_mov_b32_e32 v24, v139
	v_mov_b32_e32 v25, v139
	v_mov_b32_e32 v26, v139
	v_mov_b32_e32 v27, v139
	v_mov_b32_e32 v28, v139
	v_mov_b32_e32 v29, v139
	v_mov_b32_e32 v30, v139
	v_mov_b32_e32 v31, v139
	v_mov_b32_e32 v32, v139
	v_mov_b32_e32 v33, v139
	v_mov_b32_e32 v34, v139
	v_mov_b32_e32 v35, v139
	v_mov_b32_e32 v36, v139
	v_mov_b32_e32 v37, v139
	v_mov_b32_e32 v38, v139
	v_mov_b32_e32 v39, v139
	v_mov_b32_e32 v40, v139
	v_mov_b32_e32 v41, v139
	v_mov_b32_e32 v42, v139
	v_mov_b32_e32 v43, v139
	v_mov_b32_e32 v44, v139
	v_mov_b32_e32 v45, v139
	v_mov_b32_e32 v46, v139
	v_mov_b32_e32 v48, v139
	v_mov_b32_e32 v49, v139
	v_mov_b32_e32 v50, v139
	v_mov_b32_e32 v51, v139
	v_mov_b32_e32 v52, v139
	v_mov_b32_e32 v53, v139
	v_mov_b32_e32 v54, v139
	v_mov_b32_e32 v55, v139
	v_mov_b32_e32 v56, v139
	v_mov_b32_e32 v57, v139
	v_mov_b32_e32 v58, v139
	v_mov_b32_e32 v59, v139
	v_mov_b32_e32 v60, v139
	v_mov_b32_e32 v61, v139
	v_mov_b32_e32 v62, v139
	v_mov_b32_e32 v63, v139
	v_mov_b32_e32 v64, v139
	v_mov_b32_e32 v65, v139
	v_mov_b32_e32 v66, v139
	v_mov_b32_e32 v67, v139
	v_mov_b32_e32 v68, v139
	v_mov_b32_e32 v69, v139
	v_mov_b32_e32 v70, v139
	v_mov_b32_e32 v72, v139
	v_mov_b32_e32 v73, v139
	v_mov_b32_e32 v74, v139
	v_mov_b32_e32 v75, v139
	v_mov_b32_e32 v76, v139
	v_mov_b32_e32 v77, v139
	v_mov_b32_e32 v78, v139
	v_mov_b32_e32 v79, v139
	v_mov_b32_e32 v80, v139
	v_mov_b32_e32 v81, v139
	v_mov_b32_e32 v82, v139
	v_mov_b32_e32 v83, v139
	v_mov_b32_e32 v84, v139
	v_mov_b32_e32 v86, v139
	v_mov_b32_e32 v87, v139
	v_mov_b32_e32 v88, v139
	v_mov_b32_e32 v89, v139
	v_mov_b32_e32 v90, v139
	v_mov_b32_e32 v92, v139
	v_mov_b32_e32 v93, v139
	v_mov_b32_e32 v94, v139
	v_mov_b32_e32 v95, v139
	v_mov_b32_e32 v96, v139
	s_branch .Lqkv_w03_afterbar

.Lqkv_w03_afterbar:
	v_add_u32_e32 v110, s2, v1
	v_add_u32_e32 v134, s2, v152
	ds_read_b128 v[98:101], v110
	ds_read_b128 v[102:105], v110 offset:1024
	ds_read_b128 v[106:109], v110 offset:2048
	ds_read_b128 v[110:113], v110 offset:3072
	ds_read_b128 v[114:117], v134 offset:16384
	ds_read_b128 v[118:121], v134 offset:17408
	ds_read_b128 v[122:125], v134 offset:18432
	ds_read_b128 v[126:129], v134 offset:19456
	ds_read_b128 v[130:133], v134 offset:20480
	ds_read_b128 v[134:137], v134 offset:21504
	s_addk_i32 s2, 0x7000
	s_barrier
	s_setprio 1
	s_waitcnt lgkmcnt(5)
	v_mfma_f32_16x16x32_f16 v[94:97], v[114:117], v[98:101], v[94:97]
	s_cmp_lg_u32 s2, 0x23000
	s_cselect_b32 s2, s2, 0
	s_waitcnt lgkmcnt(4)
	v_mfma_f32_16x16x32_f16 v[90:93], v[118:121], v[98:101], v[90:93]
	s_waitcnt lgkmcnt(3)
	v_mfma_f32_16x16x32_f16 v[86:89], v[122:125], v[98:101], v[86:89]
	s_waitcnt lgkmcnt(2)
	v_mfma_f32_16x16x32_f16 v[82:85], v[126:129], v[98:101], v[82:85]
	s_waitcnt lgkmcnt(1)
	v_mfma_f32_16x16x32_f16 v[78:81], v[130:133], v[98:101], v[78:81]
	s_waitcnt lgkmcnt(0)
	v_mfma_f32_16x16x32_f16 v[74:77], v[134:137], v[98:101], v[74:77]
	v_mfma_f32_16x16x32_f16 v[70:73], v[114:117], v[102:105], v[70:73]
	v_mfma_f32_16x16x32_f16 v[66:69], v[118:121], v[102:105], v[66:69]
	v_mfma_f32_16x16x32_f16 v[62:65], v[122:125], v[102:105], v[62:65]
	v_mfma_f32_16x16x32_f16 v[58:61], v[126:129], v[102:105], v[58:61]
	v_mfma_f32_16x16x32_f16 v[54:57], v[130:133], v[102:105], v[54:57]
	v_mfma_f32_16x16x32_f16 v[50:53], v[134:137], v[102:105], v[50:53]
	v_mfma_f32_16x16x32_f16 v[46:49], v[114:117], v[106:109], v[46:49]
	v_mfma_f32_16x16x32_f16 v[42:45], v[118:121], v[106:109], v[42:45]
	v_mfma_f32_16x16x32_f16 v[38:41], v[122:125], v[106:109], v[38:41]
	v_mfma_f32_16x16x32_f16 v[34:37], v[126:129], v[106:109], v[34:37]
	v_mfma_f32_16x16x32_f16 v[30:33], v[130:133], v[106:109], v[30:33]
	v_mfma_f32_16x16x32_f16 v[26:29], v[134:137], v[106:109], v[26:29]
	v_mfma_f32_16x16x32_f16 v[22:25], v[114:117], v[110:113], v[22:25]
	v_mfma_f32_16x16x32_f16 v[18:21], v[118:121], v[110:113], v[18:21]
	v_mfma_f32_16x16x32_f16 v[14:17], v[122:125], v[110:113], v[14:17]
	v_mfma_f32_16x16x32_f16 v[10:13], v[126:129], v[110:113], v[10:13]
	v_mfma_f32_16x16x32_f16 v[6:9], v[130:133], v[110:113], v[6:9]
	v_mfma_f32_16x16x32_f16 v[2:5], v[134:137], v[110:113], v[2:5]
	s_setprio 0
	s_waitcnt lgkmcnt(0)
	s_waitcnt lgkmcnt(0)
	s_barrier
	v_add_u32_e32 v110, s2, v1
	v_add_u32_e32 v134, s2, v152
	ds_read_b128 v[98:101], v110
	ds_read_b128 v[102:105], v110 offset:1024
	ds_read_b128 v[106:109], v110 offset:2048
	ds_read_b128 v[110:113], v110 offset:3072
	ds_read_b128 v[114:117], v134 offset:16384
	ds_read_b128 v[118:121], v134 offset:17408
	ds_read_b128 v[122:125], v134 offset:18432
	ds_read_b128 v[126:129], v134 offset:19456
	ds_read_b128 v[130:133], v134 offset:20480
	ds_read_b128 v[134:137], v134 offset:21504
	s_addk_i32 s2, 0x7000
	s_barrier
	s_setprio 1
	s_waitcnt lgkmcnt(5)
	v_mfma_f32_16x16x32_f16 v[94:97], v[114:117], v[98:101], v[94:97]
	s_cmp_lg_u32 s2, 0x23000
	s_cselect_b32 s2, s2, 0
	s_waitcnt lgkmcnt(4)
	v_mfma_f32_16x16x32_f16 v[90:93], v[118:121], v[98:101], v[90:93]
	s_waitcnt lgkmcnt(3)
	v_mfma_f32_16x16x32_f16 v[86:89], v[122:125], v[98:101], v[86:89]
	s_waitcnt lgkmcnt(2)
	v_mfma_f32_16x16x32_f16 v[82:85], v[126:129], v[98:101], v[82:85]
	s_waitcnt lgkmcnt(1)
	v_mfma_f32_16x16x32_f16 v[78:81], v[130:133], v[98:101], v[78:81]
	s_waitcnt lgkmcnt(0)
	v_mfma_f32_16x16x32_f16 v[74:77], v[134:137], v[98:101], v[74:77]
	v_mfma_f32_16x16x32_f16 v[70:73], v[114:117], v[102:105], v[70:73]
	v_mfma_f32_16x16x32_f16 v[66:69], v[118:121], v[102:105], v[66:69]
	v_mfma_f32_16x16x32_f16 v[62:65], v[122:125], v[102:105], v[62:65]
	v_mfma_f32_16x16x32_f16 v[58:61], v[126:129], v[102:105], v[58:61]
	v_mfma_f32_16x16x32_f16 v[54:57], v[130:133], v[102:105], v[54:57]
	v_mfma_f32_16x16x32_f16 v[50:53], v[134:137], v[102:105], v[50:53]
	v_mfma_f32_16x16x32_f16 v[46:49], v[114:117], v[106:109], v[46:49]
	v_mfma_f32_16x16x32_f16 v[42:45], v[118:121], v[106:109], v[42:45]
	v_mfma_f32_16x16x32_f16 v[38:41], v[122:125], v[106:109], v[38:41]
	v_mfma_f32_16x16x32_f16 v[34:37], v[126:129], v[106:109], v[34:37]
	v_mfma_f32_16x16x32_f16 v[30:33], v[130:133], v[106:109], v[30:33]
	v_mfma_f32_16x16x32_f16 v[26:29], v[134:137], v[106:109], v[26:29]
	v_mfma_f32_16x16x32_f16 v[22:25], v[114:117], v[110:113], v[22:25]
	v_mfma_f32_16x16x32_f16 v[18:21], v[118:121], v[110:113], v[18:21]
	v_mfma_f32_16x16x32_f16 v[14:17], v[122:125], v[110:113], v[14:17]
	v_mfma_f32_16x16x32_f16 v[10:13], v[126:129], v[110:113], v[10:13]
	v_mfma_f32_16x16x32_f16 v[6:9], v[130:133], v[110:113], v[6:9]
	v_mfma_f32_16x16x32_f16 v[2:5], v[134:137], v[110:113], v[2:5]
	s_setprio 0
	s_add_i32 s17, s17, -2
	s_cmp_eq_u32 s17, 0
	s_cbranch_scc0 .LBB1_13

.LBB3_1:
	s_waitcnt vmcnt(3) lgkmcnt(0)
	s_barrier
	s_add_u32 s34, s20, s28
	s_addc_u32 s35, s21, s27
	s_add_i32 s31, s30, s23
	s_waitcnt lgkmcnt(3)
	v_mfma_f32_16x16x32_f16 v[92:95], v[20:23], v[28:31], v[92:95]
	v_mfma_f32_16x16x32_f16 v[72:75], v[20:23], v[24:27], v[72:75]
	s_mov_b32 m0, s31
	s_nop 0
	global_load_lds_dwordx4 v100, s[14:15]
	s_addk_i32 s31, 0x400
	v_mfma_f32_16x16x32_f16 v[56:59], v[20:23], v[16:19], v[56:59]
	v_mfma_f32_16x16x32_f16 v[20:23], v[20:23], v[0:3], v[40:43]
	s_mov_b32 m0, s31
	s_nop 0
	global_load_lds_dwordx4 v99, s[14:15]
	s_add_i32 s33, s30, s26
	s_addk_i32 s30, 0x6000
	s_nop 2
	v_add_u32_e32 v41, s29, v103
	s_waitcnt lgkmcnt(2)
	v_mfma_f32_16x16x32_f16 v[88:91], v[12:15], v[28:31], v[88:91]
	s_mov_b32 m0, s33
	s_nop 0
	global_load_lds_dwordx4 v102, s[34:35]
	v_add_u32_e32 v40, s29, v98
	s_addk_i32 s29, 0x6000
	s_cmp_lg_u32 s30, 0x18000
	s_waitcnt lgkmcnt(1)
	v_mfma_f32_16x16x32_f16 v[80:83], v[8:11], v[28:31], v[80:83]
	s_cselect_b32 s33, s30, 0
	s_cmp_lg_u32 s29, 0x18000
	s_cselect_b32 s29, s29, 0
	s_waitcnt lgkmcnt(0)
	v_mfma_f32_16x16x32_f16 v[28:31], v[4:7], v[28:31], v[76:79]
	s_add_u32 s30, s14, 0x80000
	s_addc_u32 s31, s15, 0
	s_add_u32 s34, s20, s18
	v_mfma_f32_16x16x32_f16 v[68:71], v[12:15], v[24:27], v[68:71]
	s_addc_u32 s35, s21, s19
	s_add_i32 s36, s33, s23
	v_add_u32_e32 v116, s29, v98
	v_mfma_f32_16x16x32_f16 v[64:67], v[8:11], v[24:27], v[64:67]
	v_add_u32_e32 v117, s29, v103
	s_add_i32 s37, s33, s26
	s_addk_i32 s33, 0x6000
	v_mfma_f32_16x16x32_f16 v[24:27], v[4:7], v[24:27], v[60:63]
	s_addk_i32 s29, 0x6000
	v_mfma_f32_16x16x32_f16 v[48:51], v[12:15], v[16:19], v[48:51]
	v_mfma_f32_16x16x32_f16 v[52:55], v[8:11], v[16:19], v[52:55]
	v_mfma_f32_16x16x32_f16 v[16:19], v[4:7], v[16:19], v[44:47]
	v_mfma_f32_16x16x32_f16 v[36:39], v[12:15], v[0:3], v[36:39]
	v_mfma_f32_16x16x32_f16 v[32:35], v[8:11], v[0:3], v[32:35]
	v_mfma_f32_16x16x32_f16 v[84:87], v[4:7], v[0:3], v[84:87]
	ds_read_b128 v[0:3], v41 offset:16384
	ds_read_b128 v[4:7], v41 offset:17408
	ds_read_b128 v[8:11], v40
	ds_read_b128 v[12:15], v40 offset:1024
	ds_read_b128 v[104:107], v41 offset:18432
	ds_read_b128 v[108:111], v41 offset:19456
	s_waitcnt lgkmcnt(3)
	v_mfma_f32_16x16x32_f16 v[92:95], v[0:3], v[8:11], v[92:95]
	v_mfma_f32_16x16x32_f16 v[88:91], v[4:7], v[8:11], v[88:91]
	s_waitcnt lgkmcnt(1)
	v_mfma_f32_16x16x32_f16 v[80:83], v[104:107], v[8:11], v[80:83]
	s_waitcnt lgkmcnt(0)
	v_mfma_f32_16x16x32_f16 v[76:79], v[108:111], v[8:11], v[28:31]
	ds_read_b128 v[8:11], v40 offset:2048
	ds_read_b128 v[112:115], v40 offset:3072
	s_waitcnt vmcnt(3) lgkmcnt(0)
	s_barrier
	v_mfma_f32_16x16x32_f16 v[72:75], v[0:3], v[12:15], v[72:75]
	v_mfma_f32_16x16x32_f16 v[68:71], v[4:7], v[12:15], v[68:71]
	s_mov_b32 m0, s36
	s_nop 0
	global_load_lds_dwordx4 v100, s[30:31]
	s_addk_i32 s36, 0x400
	v_mfma_f32_16x16x32_f16 v[64:67], v[104:107], v[12:15], v[64:67]
	v_mfma_f32_16x16x32_f16 v[60:63], v[108:111], v[12:15], v[24:27]
	s_mov_b32 m0, s36
	s_nop 0
	global_load_lds_dwordx4 v99, s[30:31]
	s_cmp_lg_u32 s33, 0x18000
	s_cselect_b32 s30, s33, 0
	s_cmp_lg_u32 s29, 0x18000
	s_cselect_b32 s29, s29, 0
	s_add_i32 s13, s13, 2
	s_add_u32 s14, s14, 0x100000
	s_addc_u32 s15, s15, 0
	s_add_u32 s20, s20, s16
	s_addc_u32 s21, s21, s17
	s_waitcnt lgkmcnt(1)
	v_mfma_f32_16x16x32_f16 v[56:59], v[0:3], v[8:11], v[56:59]
	v_mfma_f32_16x16x32_f16 v[44:47], v[108:111], v[8:11], v[16:19]
	s_mov_b32 m0, s37
	s_nop 0
	global_load_lds_dwordx4 v102, s[34:35]
	s_cmp_gt_u32 s13, 25
	ds_read_b128 v[28:31], v116
	ds_read_b128 v[24:27], v116 offset:1024
	s_nop 0
	ds_read_b128 v[16:19], v116 offset:2048
	s_waitcnt lgkmcnt(3)
	v_mfma_f32_16x16x32_f16 v[40:43], v[0:3], v[112:115], v[20:23]
	ds_read_b128 v[0:3], v116 offset:3072
	s_nop 1
	ds_read_b128 v[20:23], v117 offset:16384
	ds_read_b128 v[12:15], v117 offset:17408
	v_mfma_f32_16x16x32_f16 v[48:51], v[4:7], v[8:11], v[48:51]
	v_mfma_f32_16x16x32_f16 v[52:55], v[104:107], v[8:11], v[52:55]
	v_mfma_f32_16x16x32_f16 v[36:39], v[4:7], v[112:115], v[36:39]
	ds_read_b128 v[8:11], v117 offset:18432
	ds_read_b128 v[4:7], v117 offset:19456
	v_mfma_f32_16x16x32_f16 v[32:35], v[104:107], v[112:115], v[32:35]
	v_mfma_f32_16x16x32_f16 v[84:87], v[108:111], v[112:115], v[84:87]
	s_cbranch_scc0 .LBB3_1
	s_lshl_b32 s13, s24, 8
	s_add_u32 s4, s4, 0xf80000
	s_addc_u32 s5, s5, 0
	s_mul_i32 s15, s12, 0x7c0
	s_waitcnt vmcnt(3) lgkmcnt(0)
	s_barrier
	s_mul_hi_i32 s14, s12, 0x7c0
	s_add_u32 s6, s6, s15
	s_addc_u32 s7, s7, s14
	s_add_i32 s14, s23, 0x12000
	s_mov_b32 s15, m0
	s_mov_b32 m0, s14
	s_nop 0
	global_load_lds_dwordx4 v100, s[4:5]
	s_mov_b32 m0, s15
	s_add_i32 s23, s23, 0x12400
	s_mov_b32 s14, m0
	s_mov_b32 m0, s23
	s_nop 0
	global_load_lds_dwordx4 v99, s[4:5]
	s_mov_b32 m0, s14
	s_add_i32 s25, s25, 0x16000
	s_mov_b32 s4, m0
	s_mov_b32 m0, s25
	s_nop 0
	global_load_lds_dwordx4 v102, s[6:7]
	s_mov_b32 m0, s4
	s_waitcnt lgkmcnt(3)
	v_mfma_f32_16x16x32_f16 v[92:95], v[20:23], v[28:31], v[92:95]
	v_lshlrev_b32_e32 v97, 3, v97
	v_and_or_b32 v97, v97, 24, s22
	v_or_b32_e32 v126, s2, v97
	s_waitcnt lgkmcnt(2)
	v_mfma_f32_16x16x32_f16 v[88:91], v[12:15], v[28:31], v[88:91]
	v_ashrrev_i32_e32 v127, 31, v126
	v_add_u32_e32 v99, 0x12400, v101
	v_add_u32_e32 v122, 0x12c00, v101
	s_waitcnt lgkmcnt(1)
	v_mfma_f32_16x16x32_f16 v[80:83], v[8:11], v[28:31], v[80:83]
	v_lshlrev_b64 v[138:139], 2, v[126:127]
	v_lshl_add_u64 v[134:135], s[10:11], 0, v[138:139]
	s_load_dword s0, s[0:1], 0x2c
	s_waitcnt lgkmcnt(0)
	v_mfma_f32_16x16x32_f16 v[28:31], v[4:7], v[28:31], v[76:79]
	s_add_i32 s3, s3, s13
	v_or_b32_e32 v140, s3, v96
	v_mad_i64_i32 v[96:97], s[2:3], v140, s12, 0
	v_mfma_f32_16x16x32_f16 v[72:75], v[20:23], v[24:27], v[72:75]
	v_lshl_add_u64 v[96:97], v[96:97], 2, s[8:9]
	v_lshl_add_u64 v[96:97], v[96:97], 0, v[138:139]
	v_mfma_f32_16x16x32_f16 v[68:71], v[12:15], v[24:27], v[68:71]
	v_mfma_f32_16x16x32_f16 v[64:67], v[8:11], v[24:27], v[64:67]
	v_mfma_f32_16x16x32_f16 v[24:27], v[4:7], v[24:27], v[60:63]
	v_mfma_f32_16x16x32_f16 v[56:59], v[20:23], v[16:19], v[56:59]
	v_mfma_f32_16x16x32_f16 v[48:51], v[12:15], v[16:19], v[48:51]
	v_mfma_f32_16x16x32_f16 v[52:55], v[8:11], v[16:19], v[52:55]
	v_mfma_f32_16x16x32_f16 v[16:19], v[4:7], v[16:19], v[44:47]
	v_mfma_f32_16x16x32_f16 v[20:23], v[20:23], v[0:3], v[40:43]
	v_mfma_f32_16x16x32_f16 v[12:15], v[12:15], v[0:3], v[36:39]
	v_mfma_f32_16x16x32_f16 v[8:11], v[8:11], v[0:3], v[32:35]
	s_nop 2
	ds_read_b128 v[32:35], v103 offset:40960
	ds_read_b128 v[36:39], v103 offset:41984
	v_mfma_f32_16x16x32_f16 v[0:3], v[4:7], v[0:3], v[84:87]
	ds_read_b128 v[4:7], v98 offset:24576
	ds_read_b128 v[40:43], v98 offset:25600
	ds_read_b128 v[60:63], v103 offset:43008
	ds_read_b128 v[84:87], v103 offset:44032
	s_waitcnt lgkmcnt(3)
	v_mfma_f32_16x16x32_f16 v[44:47], v[32:35], v[4:7], v[92:95]
	v_mfma_f32_16x16x32_f16 v[76:79], v[36:39], v[4:7], v[88:91]
	s_waitcnt lgkmcnt(1)
	v_mfma_f32_16x16x32_f16 v[80:83], v[60:63], v[4:7], v[80:83]
	s_waitcnt lgkmcnt(0)
	v_mfma_f32_16x16x32_f16 v[28:31], v[84:87], v[4:7], v[28:31]
	v_mfma_f32_16x16x32_f16 v[72:75], v[32:35], v[40:43], v[72:75]
	v_mfma_f32_16x16x32_f16 v[68:71], v[36:39], v[40:43], v[68:71]
	v_mfma_f32_16x16x32_f16 v[64:67], v[60:63], v[40:43], v[64:67]
	v_mfma_f32_16x16x32_f16 v[24:27], v[84:87], v[40:43], v[24:27]
	ds_read_b128 v[4:7], v98 offset:26624
	ds_read_b128 v[40:43], v98 offset:27648
	s_waitcnt vmcnt(3) lgkmcnt(0)
	s_barrier
	s_waitcnt lgkmcnt(1)
	v_mfma_f32_16x16x32_f16 v[56:59], v[32:35], v[4:7], v[56:59]
	s_waitcnt lgkmcnt(0)
	v_mfma_f32_16x16x32_f16 v[20:23], v[32:35], v[40:43], v[20:23]
	ds_read_b128 v[32:35], v101 offset:49152
	v_mfma_f32_16x16x32_f16 v[48:51], v[36:39], v[4:7], v[48:51]
	v_mfma_f32_16x16x32_f16 v[52:55], v[60:63], v[4:7], v[52:55]
	v_mfma_f32_16x16x32_f16 v[16:19], v[84:87], v[4:7], v[16:19]
	v_mfma_f32_16x16x32_f16 v[12:15], v[36:39], v[40:43], v[12:15]
	v_mfma_f32_16x16x32_f16 v[36:39], v[60:63], v[40:43], v[8:11]
	ds_read_b128 v[60:63], v98 offset:49152
	ds_read_b128 v[88:91], v98 offset:50176
	ds_read_b128 v[92:95], v101 offset:50176
	v_mfma_f32_16x16x32_f16 v[4:7], v[84:87], v[40:43], v[0:3]
	ds_read_b128 v[40:43], v98 offset:51200
	ds_read_b128 v[8:11], v98 offset:52224
	ds_read_b128 v[84:87], v101 offset:51200
	ds_read_b128 v[102:105], v101 offset:52224
	s_waitcnt vmcnt(0) lgkmcnt(0)
	s_barrier
	v_add_u32_e32 v0, 0x12000, v98
	v_add_u32_e32 v1, 0x12400, v98
	ds_read_b128 v[106:109], v0
	ds_read_b128 v[110:113], v1
	v_add_u32_e32 v0, 0x12800, v98
	v_add_u32_e32 v1, 0x12c00, v98
	v_add_u32_e32 v98, 0x12000, v101
	s_waitcnt lgkmcnt(8)
	v_mfma_f32_16x16x32_f16 v[44:47], v[32:35], v[60:63], v[44:47]
	ds_read_b128 v[114:117], v0
	ds_read_b128 v[0:3], v1
	s_waitcnt lgkmcnt(8)
	v_mfma_f32_16x16x32_f16 v[76:79], v[92:95], v[60:63], v[76:79]
	s_waitcnt lgkmcnt(5)
	v_mfma_f32_16x16x32_f16 v[80:83], v[84:87], v[60:63], v[80:83]
	s_waitcnt lgkmcnt(4)
	v_mfma_f32_16x16x32_f16 v[28:31], v[102:105], v[60:63], v[28:31]
	ds_read_b128 v[60:63], v98
	ds_read_b128 v[118:121], v99
	v_add_u32_e32 v98, 0x12800, v101
	ds_read_b128 v[98:101], v98
	ds_read_b128 v[122:125], v122
	s_waitcnt vmcnt(0) lgkmcnt(0)
	s_barrier
	global_load_dwordx4 v[148:151], v[134:135], off
	global_load_dwordx4 v[152:155], v[134:135], off offset:16
	global_load_dwordx4 v[156:159], v[134:135], off offset:128
	global_load_dwordx4 v[160:163], v[134:135], off offset:144
	v_and_b32_e32 v141, 24, v126
	v_lshlrev_b32_e32 v141, 1, v141
	v_sub_u32_e32 v138, v138, v141
	v_mfma_f32_16x16x32_f16 v[72:75], v[32:35], v[88:91], v[72:75]
	v_mfma_f32_16x16x32_f16 v[68:71], v[92:95], v[88:91], v[68:71]
	v_mfma_f32_16x16x32_f16 v[64:67], v[84:87], v[88:91], v[64:67]
	v_mfma_f32_16x16x32_f16 v[24:27], v[102:105], v[88:91], v[24:27]
	v_mfma_f32_16x16x32_f16 v[56:59], v[32:35], v[40:43], v[56:59]
	v_mfma_f32_16x16x32_f16 v[48:51], v[92:95], v[40:43], v[48:51]
	v_mfma_f32_16x16x32_f16 v[52:55], v[84:87], v[40:43], v[52:55]
	v_mfma_f32_16x16x32_f16 v[16:19], v[102:105], v[40:43], v[16:19]
	v_mfma_f32_16x16x32_f16 v[20:23], v[32:35], v[8:11], v[20:23]
	v_mfma_f32_16x16x32_f16 v[12:15], v[92:95], v[8:11], v[12:15]
	v_mfma_f32_16x16x32_f16 v[36:39], v[84:87], v[8:11], v[36:39]
	v_mfma_f32_16x16x32_f16 v[4:7], v[102:105], v[8:11], v[4:7]
	v_mad_i64_i32 v[96:97], s[2:3], v140, s12, 0
	v_lshl_add_u64 v[96:97], v[96:97], 2, s[8:9]
	v_lshl_add_u64 v[96:97], v[96:97], 0, v[138:139]
	v_or_b32_e32 v141, 16, v140
	v_mad_i64_i32 v[142:143], s[2:3], v141, s12, 0
	v_lshl_add_u64 v[142:143], v[142:143], 2, s[8:9]
	v_lshl_add_u64 v[142:143], v[142:143], 0, v[138:139]
	v_or_b32_e32 v141, 32, v140
	v_mad_i64_i32 v[144:145], s[2:3], v141, s12, 0
	v_lshl_add_u64 v[144:145], v[144:145], 2, s[8:9]
	v_lshl_add_u64 v[144:145], v[144:145], 0, v[138:139]
	v_or_b32_e32 v141, 48, v140
	v_mad_i64_i32 v[146:147], s[2:3], v141, s12, 0
	v_lshl_add_u64 v[146:147], v[146:147], 2, s[8:9]
	v_lshl_add_u64 v[146:147], v[146:147], 0, v[138:139]
	v_mfma_f32_16x16x32_f16 v[44:47], v[60:63], v[106:109], v[44:47]
	v_mfma_f32_16x16x32_f16 v[76:79], v[118:121], v[106:109], v[76:79]
	v_mfma_f32_16x16x32_f16 v[80:83], v[98:101], v[106:109], v[80:83]
	v_mfma_f32_16x16x32_f16 v[28:31], v[122:125], v[106:109], v[28:31]
	v_mfma_f32_16x16x32_f16 v[72:75], v[60:63], v[110:113], v[72:75]
	v_mfma_f32_16x16x32_f16 v[68:71], v[118:121], v[110:113], v[68:71]
	v_mfma_f32_16x16x32_f16 v[64:67], v[98:101], v[110:113], v[64:67]
	v_mfma_f32_16x16x32_f16 v[24:27], v[122:125], v[110:113], v[24:27]
	v_mfma_f32_16x16x32_f16 v[56:59], v[60:63], v[114:117], v[56:59]
	v_mfma_f32_16x16x32_f16 v[48:51], v[118:121], v[114:117], v[48:51]
	v_mfma_f32_16x16x32_f16 v[52:55], v[98:101], v[114:117], v[52:55]
	v_mfma_f32_16x16x32_f16 v[16:19], v[122:125], v[114:117], v[16:19]
	v_mfma_f32_16x16x32_f16 v[20:23], v[60:63], v[0:3], v[20:23]
	v_mfma_f32_16x16x32_f16 v[12:15], v[118:121], v[0:3], v[12:15]
	v_mfma_f32_16x16x32_f16 v[36:39], v[98:101], v[0:3], v[36:39]
	v_mfma_f32_16x16x32_f16 v[4:7], v[122:125], v[0:3], v[4:7]
	s_waitcnt vmcnt(0)
	v_pk_fma_f32 v[44:45], s[0:1], v[44:45], v[148:149] op_sel_hi:[0,1,1]
	v_pk_fma_f32 v[46:47], s[0:1], v[46:47], v[150:151] op_sel_hi:[0,1,1]
	v_pk_fma_f32 v[76:77], s[0:1], v[76:77], v[152:153] op_sel_hi:[0,1,1]
	v_pk_fma_f32 v[78:79], s[0:1], v[78:79], v[154:155] op_sel_hi:[0,1,1]
	v_pk_fma_f32 v[80:81], s[0:1], v[80:81], v[156:157] op_sel_hi:[0,1,1]
	v_pk_fma_f32 v[82:83], s[0:1], v[82:83], v[158:159] op_sel_hi:[0,1,1]
	v_pk_fma_f32 v[28:29], s[0:1], v[28:29], v[160:161] op_sel_hi:[0,1,1]
	v_pk_fma_f32 v[30:31], s[0:1], v[30:31], v[162:163] op_sel_hi:[0,1,1]
	s_nop 1
	v_permlane16_swap_b32_e32 v44, v76
	v_permlane16_swap_b32_e32 v45, v77
	v_permlane16_swap_b32_e32 v46, v78
	v_permlane16_swap_b32_e32 v47, v79
	v_permlane16_swap_b32_e32 v80, v28
	v_permlane16_swap_b32_e32 v81, v29
	v_permlane16_swap_b32_e32 v82, v30
	v_permlane16_swap_b32_e32 v83, v31
	v_permlane32_swap_b32_e32 v44, v76
	v_permlane32_swap_b32_e32 v45, v77
	v_permlane32_swap_b32_e32 v46, v78
	v_permlane32_swap_b32_e32 v47, v79
	v_permlane32_swap_b32_e32 v80, v28
	v_permlane32_swap_b32_e32 v81, v29
	v_permlane32_swap_b32_e32 v82, v30
	v_permlane32_swap_b32_e32 v83, v31
	global_store_dwordx4 v[96:97], v[44:47], off sc1
	global_store_dwordx4 v[96:97], v[76:79], off offset:64 sc1
	global_store_dwordx4 v[96:97], v[80:83], off offset:128 sc1
	global_store_dwordx4 v[96:97], v[28:31], off offset:192 sc1
	v_pk_fma_f32 v[72:73], s[0:1], v[72:73], v[148:149] op_sel_hi:[0,1,1]
	v_pk_fma_f32 v[74:75], s[0:1], v[74:75], v[150:151] op_sel_hi:[0,1,1]
	v_pk_fma_f32 v[68:69], s[0:1], v[68:69], v[152:153] op_sel_hi:[0,1,1]
	v_pk_fma_f32 v[70:71], s[0:1], v[70:71], v[154:155] op_sel_hi:[0,1,1]
	v_pk_fma_f32 v[64:65], s[0:1], v[64:65], v[156:157] op_sel_hi:[0,1,1]
	v_pk_fma_f32 v[66:67], s[0:1], v[66:67], v[158:159] op_sel_hi:[0,1,1]
	v_pk_fma_f32 v[24:25], s[0:1], v[24:25], v[160:161] op_sel_hi:[0,1,1]
	v_pk_fma_f32 v[26:27], s[0:1], v[26:27], v[162:163] op_sel_hi:[0,1,1]
	s_nop 1
	v_permlane16_swap_b32_e32 v72, v68
	v_permlane16_swap_b32_e32 v73, v69
	v_permlane16_swap_b32_e32 v74, v70
	v_permlane16_swap_b32_e32 v75, v71
	v_permlane16_swap_b32_e32 v64, v24
	v_permlane16_swap_b32_e32 v65, v25
	v_permlane16_swap_b32_e32 v66, v26
	v_permlane16_swap_b32_e32 v67, v27
	v_permlane32_swap_b32_e32 v72, v68
	v_permlane32_swap_b32_e32 v73, v69
	v_permlane32_swap_b32_e32 v74, v70
	v_permlane32_swap_b32_e32 v75, v71
	v_permlane32_swap_b32_e32 v64, v24
	v_permlane32_swap_b32_e32 v65, v25
	v_permlane32_swap_b32_e32 v66, v26
	v_permlane32_swap_b32_e32 v67, v27
	global_store_dwordx4 v[142:143], v[72:75], off sc1
	global_store_dwordx4 v[142:143], v[68:71], off offset:64 sc1
	global_store_dwordx4 v[142:143], v[64:67], off offset:128 sc1
	global_store_dwordx4 v[142:143], v[24:27], off offset:192 sc1
	v_pk_fma_f32 v[56:57], s[0:1], v[56:57], v[148:149] op_sel_hi:[0,1,1]
	v_pk_fma_f32 v[58:59], s[0:1], v[58:59], v[150:151] op_sel_hi:[0,1,1]
	v_pk_fma_f32 v[48:49], s[0:1], v[48:49], v[152:153] op_sel_hi:[0,1,1]
	v_pk_fma_f32 v[50:51], s[0:1], v[50:51], v[154:155] op_sel_hi:[0,1,1]
	v_pk_fma_f32 v[52:53], s[0:1], v[52:53], v[156:157] op_sel_hi:[0,1,1]
	v_pk_fma_f32 v[54:55], s[0:1], v[54:55], v[158:159] op_sel_hi:[0,1,1]
	v_pk_fma_f32 v[16:17], s[0:1], v[16:17], v[160:161] op_sel_hi:[0,1,1]
	v_pk_fma_f32 v[18:19], s[0:1], v[18:19], v[162:163] op_sel_hi:[0,1,1]
	s_nop 1
	v_permlane16_swap_b32_e32 v56, v48
	v_permlane16_swap_b32_e32 v57, v49
	v_permlane16_swap_b32_e32 v58, v50
	v_permlane16_swap_b32_e32 v59, v51
	v_permlane16_swap_b32_e32 v52, v16
	v_permlane16_swap_b32_e32 v53, v17
	v_permlane16_swap_b32_e32 v54, v18
	v_permlane16_swap_b32_e32 v55, v19
	v_permlane32_swap_b32_e32 v56, v48
	v_permlane32_swap_b32_e32 v57, v49
	v_permlane32_swap_b32_e32 v58, v50
	v_permlane32_swap_b32_e32 v59, v51
	v_permlane32_swap_b32_e32 v52, v16
	v_permlane32_swap_b32_e32 v53, v17
	v_permlane32_swap_b32_e32 v54, v18
	v_permlane32_swap_b32_e32 v55, v19
	global_store_dwordx4 v[144:145], v[56:59], off sc1
	global_store_dwordx4 v[144:145], v[48:51], off offset:64 sc1
	global_store_dwordx4 v[144:145], v[52:55], off offset:128 sc1
	global_store_dwordx4 v[144:145], v[16:19], off offset:192 sc1
	v_pk_fma_f32 v[20:21], s[0:1], v[20:21], v[148:149] op_sel_hi:[0,1,1]
	v_pk_fma_f32 v[22:23], s[0:1], v[22:23], v[150:151] op_sel_hi:[0,1,1]
	v_pk_fma_f32 v[12:13], s[0:1], v[12:13], v[152:153] op_sel_hi:[0,1,1]
	v_pk_fma_f32 v[14:15], s[0:1], v[14:15], v[154:155] op_sel_hi:[0,1,1]
	v_pk_fma_f32 v[36:37], s[0:1], v[36:37], v[156:157] op_sel_hi:[0,1,1]
	v_pk_fma_f32 v[38:39], s[0:1], v[38:39], v[158:159] op_sel_hi:[0,1,1]
	v_pk_fma_f32 v[4:5], s[0:1], v[4:5], v[160:161] op_sel_hi:[0,1,1]
	v_pk_fma_f32 v[6:7], s[0:1], v[6:7], v[162:163] op_sel_hi:[0,1,1]
	s_nop 1
	v_permlane16_swap_b32_e32 v20, v12
	v_permlane16_swap_b32_e32 v21, v13
	v_permlane16_swap_b32_e32 v22, v14
	v_permlane16_swap_b32_e32 v23, v15
	v_permlane16_swap_b32_e32 v36, v4
	v_permlane16_swap_b32_e32 v37, v5
	v_permlane16_swap_b32_e32 v38, v6
	v_permlane16_swap_b32_e32 v39, v7
	v_permlane32_swap_b32_e32 v20, v12
	v_permlane32_swap_b32_e32 v21, v13
	v_permlane32_swap_b32_e32 v22, v14
	v_permlane32_swap_b32_e32 v23, v15
	v_permlane32_swap_b32_e32 v36, v4
	v_permlane32_swap_b32_e32 v37, v5
	v_permlane32_swap_b32_e32 v38, v6
	v_permlane32_swap_b32_e32 v39, v7
	global_store_dwordx4 v[146:147], v[20:23], off sc1
	global_store_dwordx4 v[146:147], v[12:15], off offset:64 sc1
	global_store_dwordx4 v[146:147], v[36:39], off offset:128 sc1
	global_store_dwordx4 v[146:147], v[4:7], off offset:192 sc1
	s_endpgm
